# speedup vs baseline: 1.0035x; 1.0035x over previous
.LBB2_12:
	s_add_i32 s12, s29, -1
	s_and_b32 s30, s12, 1
	s_bitcmp1_b32 s12, 1
	s_cselect_b32 s4, 0x10001, 0
	v_lshl_add_u32 v47, s30, 17, v39
	s_lshl_b32 s31, s30, 14
	s_lshl_b64 s[10:11], s[12:13], 12
	v_add_u32_e32 v48, 0x1000, v47
	v_add_u32_e32 v49, 0x2000, v47
	v_add_u32_e32 v50, 0x3000, v47
	v_or_b32_e32 v110, s31, v34
	v_add_u32_e32 v111, s31, v121
	v_lshl_add_u64 v[112:113], v[24:25], 0, s[10:11]
	v_add_u32_e32 v124, s31, v122
	v_add_u32_e32 v125, s31, v123
	s_lshl_b32 s32, s29, 13
	s_add_i32 s32, s32, 0x4000
	s_mov_b32 s33, 0
	v_lshl_add_u64 v[114:115], v[20:21], 0, s[32:33]
	v_lshl_add_u64 v[118:119], v[22:23], 0, s[32:33]
	v_add_co_u32_e32 v116, vcc, 0x1000, v114
	v_mov_b64_e32 v[62:63], 0
	v_mov_b64_e32 v[64:65], 0
	v_addc_co_u32_e32 v117, vcc, 0, v115, vcc
	v_mov_b64_e32 v[66:67], 0
	v_mov_b64_e32 v[68:69], 0
	s_mov_b32 s31, 0
	s_sleep 1

.LBB2_20:
	s_mov_b64 exec, -1
	s_cmpk_ge_i32 s29, 0x7e
	s_waitcnt lgkmcnt(0)
	s_barrier
	ds_read_b128 v[50:53], v111
	ds_read_b128 v[54:57], v111 offset:4096
	ds_read_b128 v[58:61], v111 offset:8192
	global_store_dword v[112:113], v46, off
	ds_read_b128 v[46:49], v111 offset:12288
	ds_read_b128 v[78:81], v124
	ds_read_b128 v[82:85], v124 offset:4096
	ds_read_b128 v[86:89], v124 offset:8192
	ds_read_b128 v[90:93], v124 offset:12288
	ds_read_b128 v[94:97], v125
	ds_read_b128 v[98:101], v125 offset:4096
	ds_read_b128 v[102:105], v125 offset:8192
	ds_read_b128 v[106:109], v125 offset:12288
	v_mov_b32_e32 v29, v128
	v_mov_b32_e32 v30, v129
	v_mov_b32_e32 v31, v130
	v_mov_b32_e32 v32, v131
	v_mov_b32_e32 v33, v132
	s_cbranch_scc1 .Lrec_nopf
	global_load_ushort v128, v[114:115], off
	global_load_ushort v129, v[114:115], off offset:2048
	global_load_ushort v130, v[116:117], off
	global_load_ushort v131, v[116:117], off offset:2048
	global_load_ushort v132, v[118:119], off
.Lrec_nopf:
	v_cvt_f32_f16_e32 v112, v44
	v_cvt_f32_f16_e32 v113, v43
	v_cvt_f32_f16_e32 v114, v42
	v_cvt_f32_f16_e32 v115, v41
	v_cvt_f32_f16_e32 v118, v45
	v_cndmask_b32_e64 v116, 0, v118, s[22:23]
	v_cndmask_b32_e64 v117, v118, 0, s[22:23]
	v_smfmac_f32_16x16x64_f16 v[62:65], v[0:3], a[0:7], v28
	v_smfmac_f32_16x16x64_f16 v[66:69], v[0:3], a[128:135], v28
	v_smfmac_f32_16x16x64_f16 v[62:65], v[4:7], a[8:15], v28
	v_smfmac_f32_16x16x64_f16 v[66:69], v[4:7], a[136:143], v28
	v_smfmac_f32_16x16x64_f16 v[62:65], v[8:11], a[16:23], v28
	v_smfmac_f32_16x16x64_f16 v[66:69], v[8:11], a[144:151], v28
	v_smfmac_f32_16x16x64_f16 v[62:65], v[12:15], a[24:31], v28
	v_smfmac_f32_16x16x64_f16 v[66:69], v[12:15], a[152:159], v28
	s_waitcnt lgkmcnt(11)
	v_smfmac_f32_16x16x64_f16 v[62:65], v[50:53], a[32:39], v28
	v_smfmac_f32_16x16x64_f16 v[66:69], v[50:53], a[160:167], v28
	s_waitcnt lgkmcnt(10)
	v_smfmac_f32_16x16x64_f16 v[62:65], v[54:57], a[40:47], v28
	v_smfmac_f32_16x16x64_f16 v[66:69], v[54:57], a[168:175], v28
	s_waitcnt lgkmcnt(9)
	v_smfmac_f32_16x16x64_f16 v[62:65], v[58:61], a[48:55], v28
	v_smfmac_f32_16x16x64_f16 v[66:69], v[58:61], a[176:183], v28
	s_waitcnt lgkmcnt(8)
	v_smfmac_f32_16x16x64_f16 v[62:65], v[46:49], a[56:63], v28
	v_smfmac_f32_16x16x64_f16 v[66:69], v[46:49], a[184:191], v28
	s_waitcnt lgkmcnt(7)
	v_smfmac_f32_16x16x64_f16 v[62:65], v[78:81], a[64:71], v28
	v_smfmac_f32_16x16x64_f16 v[66:69], v[78:81], a[192:199], v28
	s_waitcnt lgkmcnt(6)
	v_smfmac_f32_16x16x64_f16 v[62:65], v[82:85], a[72:79], v28
	v_smfmac_f32_16x16x64_f16 v[66:69], v[82:85], a[200:207], v28
	s_waitcnt lgkmcnt(5)
	v_smfmac_f32_16x16x64_f16 v[62:65], v[86:89], a[80:87], v28
	v_smfmac_f32_16x16x64_f16 v[66:69], v[86:89], a[208:215], v28
	s_waitcnt lgkmcnt(4)
	v_smfmac_f32_16x16x64_f16 v[62:65], v[90:93], a[88:95], v28
	v_smfmac_f32_16x16x64_f16 v[66:69], v[90:93], a[216:223], v28
	s_waitcnt lgkmcnt(3)
	v_smfmac_f32_16x16x64_f16 v[62:65], v[94:97], a[96:103], v28
	v_smfmac_f32_16x16x64_f16 v[66:69], v[94:97], a[224:231], v28
	s_waitcnt lgkmcnt(2)
	v_smfmac_f32_16x16x64_f16 v[62:65], v[98:101], a[104:111], v28
	v_smfmac_f32_16x16x64_f16 v[66:69], v[98:101], a[232:239], v28
	s_waitcnt lgkmcnt(1)
	v_smfmac_f32_16x16x64_f16 v[62:65], v[102:105], a[112:119], v28
	v_smfmac_f32_16x16x64_f16 v[66:69], v[102:105], a[240:247], v28
	s_waitcnt lgkmcnt(0)
	v_smfmac_f32_16x16x64_f16 v[62:65], v[106:109], a[120:127], v28
	v_smfmac_f32_16x16x64_f16 v[66:69], v[106:109], a[248:255], v28
	s_nop 6
	v_permlane32_swap_b32_e32 v62, v63
	v_permlane32_swap_b32_e32 v64, v65
	v_permlane32_swap_b32_e32 v66, v67
	v_permlane32_swap_b32_e32 v68, v69
	v_add_f32_e32 v2, v62, v63
	v_add_f32_e32 v0, v64, v65
	v_add_f32_e32 v1, v66, v67
	v_add_f32_e32 v3, v68, v69

.LBB2_23:
	s_mov_b32 s32, 0x4000
	s_mov_b32 s33, 0
	v_lshl_add_u64 v[114:115], v[20:21], 0, s[32:33]
	v_lshl_add_u64 v[118:119], v[22:23], 0, s[32:33]
	v_add_co_u32_e32 v116, vcc, 0x1000, v114
	s_nop 1
	v_addc_co_u32_e32 v117, vcc, 0, v115, vcc
	global_load_ushort v128, v[114:115], off
	global_load_ushort v129, v[114:115], off offset:2048
	global_load_ushort v130, v[116:117], off
	global_load_ushort v131, v[116:117], off offset:2048
	global_load_ushort v132, v[118:119], off
	v_mov_b32_e32 v0, 0
	v_mov_b32_e32 v1, 0
	v_mov_b32_e32 v2, 0
	v_mov_b32_e32 v3, 0
	v_cvt_f32_f16_e32 v112, v44
	v_cvt_f32_f16_e32 v113, v43
	v_cvt_f32_f16_e32 v114, v42
	v_cvt_f32_f16_e32 v115, v41
	v_cvt_f32_f16_e32 v118, v45
	v_cndmask_b32_e64 v116, 0, v118, s[22:23]
	v_cndmask_b32_e64 v117, v118, 0, s[22:23]
	s_branch .Lrec_gate2

	.amdhsa_kernel _Z8lstm_recPK15HIP_vector_typeIjLj4EEPKtS4_PjS5_Pf
		.amdhsa_group_segment_fixed_size 32780
		.amdhsa_private_segment_fixed_size 0
		.amdhsa_kernarg_size 48
		.amdhsa_user_sgpr_count 2
		.amdhsa_user_sgpr_dispatch_ptr 0
		.amdhsa_user_sgpr_queue_ptr 0
		.amdhsa_user_sgpr_kernarg_segment_ptr 1
		.amdhsa_user_sgpr_dispatch_id 0
		.amdhsa_user_sgpr_kernarg_preload_length 0
		.amdhsa_user_sgpr_kernarg_preload_offset 0
		.amdhsa_user_sgpr_private_segment_size 0
		.amdhsa_uses_dynamic_stack 0
		.amdhsa_enable_private_segment 0
		.amdhsa_system_sgpr_workgroup_id_x 1
		.amdhsa_system_sgpr_workgroup_id_y 0
		.amdhsa_system_sgpr_workgroup_id_z 0
		.amdhsa_system_sgpr_workgroup_info 0
		.amdhsa_system_vgpr_workitem_id 0
		.amdhsa_next_free_vgpr 392
		.amdhsa_next_free_sgpr 96
		.amdhsa_accum_offset 136
		.amdhsa_reserve_vcc 1
		.amdhsa_float_round_mode_32 0
		.amdhsa_float_round_mode_16_64 0
		.amdhsa_float_denorm_mode_32 3
		.amdhsa_float_denorm_mode_16_64 3
		.amdhsa_dx10_clamp 1
		.amdhsa_ieee_mode 1
		.amdhsa_fp16_overflow 0
		.amdhsa_tg_split 0
		.amdhsa_exception_fp_ieee_invalid_op 0
		.amdhsa_exception_fp_denorm_src 0
		.amdhsa_exception_fp_ieee_div_zero 0
		.amdhsa_exception_fp_ieee_overflow 0
		.amdhsa_exception_fp_ieee_underflow 0
		.amdhsa_exception_fp_ieee_inexact 0
		.amdhsa_exception_int_div_zero 0
	.end_amdhsa_kernel

amdhsa.kernels:
  - .agpr_count:     0
    .args:
      - .actual_access:  read_only
        .address_space:  global
        .offset:         0
        .size:           8
        .value_kind:     global_buffer
      - .actual_access:  read_only
        .address_space:  global
        .offset:         8
        .size:           8
        .value_kind:     global_buffer
      - .actual_access:  read_only
        .address_space:  global
        .offset:         16
        .size:           8
        .value_kind:     global_buffer
      - .actual_access:  read_only
        .address_space:  global
        .offset:         24
        .size:           8
        .value_kind:     global_buffer
      - .actual_access:  read_only
        .address_space:  global
        .offset:         32
        .size:           8
        .value_kind:     global_buffer
      - .actual_access:  read_only
        .address_space:  global
        .offset:         40
        .size:           8
        .value_kind:     global_buffer
      - .actual_access:  read_only
        .address_space:  global
        .offset:         48
        .size:           8
        .value_kind:     global_buffer
      - .actual_access:  read_only
        .address_space:  global
        .offset:         56
        .size:           8
        .value_kind:     global_buffer
      - .actual_access:  read_only
        .address_space:  global
        .offset:         64
        .size:           8
        .value_kind:     global_buffer
      - .actual_access:  read_only
        .address_space:  global
        .offset:         72
        .size:           8
        .value_kind:     global_buffer
      - .actual_access:  read_only
        .address_space:  global
        .offset:         80
        .size:           8
        .value_kind:     global_buffer
      - .actual_access:  write_only
        .address_space:  global
        .offset:         88
        .size:           8
        .value_kind:     global_buffer
      - .actual_access:  write_only
        .address_space:  global
        .offset:         96
        .size:           8
        .value_kind:     global_buffer
      - .actual_access:  write_only
        .address_space:  global
        .offset:         104
        .size:           8
        .value_kind:     global_buffer
      - .actual_access:  write_only
        .address_space:  global
        .offset:         112
        .size:           8
        .value_kind:     global_buffer
      - .actual_access:  write_only
        .address_space:  global
        .offset:         120
        .size:           8
        .value_kind:     global_buffer
    .group_segment_fixed_size: 0
    .kernarg_segment_align: 8
    .kernarg_segment_size: 128
    .language:       OpenCL C
    .language_version:
      - 2
      - 0
    .max_flat_workgroup_size: 256
    .name:           _Z8pack_allPKfS0_S0_S0_S0_S0_S0_S0_S0_S0_S0_P15HIP_vector_typeIjLj4EES3_PfS3_Pj
    .private_segment_fixed_size: 0
    .sgpr_count:     28
    .sgpr_spill_count: 0
    .symbol:         _Z8pack_allPKfS0_S0_S0_S0_S0_S0_S0_S0_S0_S0_P15HIP_vector_typeIjLj4EES3_PfS3_Pj.kd
    .uniform_work_group_size: 1
    .uses_dynamic_stack: false
    .vgpr_count:     24
    .vgpr_spill_count: 0
    .wavefront_size: 64
  - .agpr_count:     0
    .args:
      - .address_space:  global
        .offset:         0
        .size:           8
        .value_kind:     global_buffer
      - .address_space:  global
        .offset:         8
        .size:           8
        .value_kind:     global_buffer
      - .actual_access:  read_only
        .address_space:  global
        .offset:         16
        .size:           8
        .value_kind:     global_buffer
      - .actual_access:  write_only
        .address_space:  global
        .offset:         24
        .size:           8
        .value_kind:     global_buffer
      - .actual_access:  write_only
        .address_space:  global
        .offset:         32
        .size:           8
        .value_kind:     global_buffer
    .group_segment_fixed_size: 0
    .kernarg_segment_align: 8
    .kernarg_segment_size: 40
    .language:       OpenCL C
    .language_version:
      - 2
      - 0
    .max_flat_workgroup_size: 512
    .name:           _Z7gemm_gxPKtS0_PKfPtS3_
    .private_segment_fixed_size: 0
    .sgpr_count:     58
    .sgpr_spill_count: 0
    .symbol:         _Z7gemm_gxPKtS0_PKfPtS3_.kd
    .uniform_work_group_size: 1
    .uses_dynamic_stack: false
    .vgpr_count:     256
    .vgpr_spill_count: 0
    .wavefront_size: 64
  - .agpr_count:     256
    .args:
      - .actual_access:  read_only
        .address_space:  global
        .offset:         0
        .size:           8
        .value_kind:     global_buffer
      - .actual_access:  read_only
        .address_space:  global
        .offset:         8
        .size:           8
        .value_kind:     global_buffer
      - .actual_access:  read_only
        .address_space:  global
        .offset:         16
        .size:           8
        .value_kind:     global_buffer
      - .address_space:  global
        .offset:         24
        .size:           8
        .value_kind:     global_buffer
      - .address_space:  global
        .offset:         32
        .size:           8
        .value_kind:     global_buffer
      - .actual_access:  write_only
        .address_space:  global
        .offset:         40
        .size:           8
        .value_kind:     global_buffer
    .group_segment_fixed_size: 32780
    .kernarg_segment_align: 8
    .kernarg_segment_size: 48
    .language:       OpenCL C
    .language_version:
      - 2
      - 0
    .max_flat_workgroup_size: 256
    .name:           _Z8lstm_recPK15HIP_vector_typeIjLj4EEPKtS4_PjS5_Pf
    .private_segment_fixed_size: 0
    .sgpr_count:     42
    .sgpr_spill_count: 0
    .symbol:         _Z8lstm_recPK15HIP_vector_typeIjLj4EEPKtS4_PjS5_Pf.kd
    .uniform_work_group_size: 1
    .uses_dynamic_stack: false
    .vgpr_count:     392
    .vgpr_spill_count: 0
    .wavefront_size: 64
